# static s_setprio 1 for waves 4-7 during the three attention phases
# speedup vs baseline: 1.0117x; 1.0033x over previous
.LBB0_253:
	v_readlane_b32 s0, v254, 0
	v_readlane_b32 s1, v254, 1
	s_load_dwordx2 s[0:1], s[0:1], 0xd8
	s_waitcnt lgkmcnt(0)
	s_cmp_lt_i32 s0, 4
	s_cselect_b64 s[0:1], -1, 0
	s_add_u32 s4, s88, 0x4ac00000
	s_addc_u32 s5, s89, 0
	v_writelane_b32 v254, s4, 49
	s_and_b64 s[0:1], s[0:1], s[2:3]
	s_andn2_b64 vcc, exec, s[0:1]
	v_writelane_b32 v254, s5, 50
	s_cbranch_vccnz .LBB0_284
	s_cmp_gt_u32 s95, 3
	s_cbranch_scc0 .Lattp_3
	s_setprio 1
.Lattp_3:
	v_mbcnt_lo_u32_b32 v0, -1, 0
	v_mbcnt_hi_u32_b32 v0, -1, v0
	s_mov_b32 s3, 0
	v_mov_b32_e32 v1, v0
	s_cmpk_gt_i32 s96, 0x83f
	s_cbranch_scc1 .LBB0_284
	s_and_b32 s2, s94, 0xffffffc0
	v_add_u32_e32 v2, s2, v1
	v_ashrrev_i32_e32 v133, 3, v2
	v_lshrrev_b32_e32 v2, 3, v1
	v_bfe_u32 v4, v1, 2, 2
	s_mov_b32 s4, 0x3fffffc
	v_and_or_b32 v2, v2, s4, v4
	v_lshlrev_b32_e32 v4, 2, v1
	v_and_b32_e32 v5, 16, v1
	v_and_or_b32 v4, v4, 12, v5
	v_lshlrev_b32_e32 v4, 1, v4
	v_lshl_or_b32 v7, v2, 6, v4
	v_bfe_u32 v4, v1, 2, 1
	v_and_b32_e32 v2, 7, v1
	v_mul_u32_u24_e32 v4, 0x1040, v4
	v_and_b32_e32 v132, 31, v1
	v_ashrrev_i32_e32 v3, 5, v1
	s_movk_i32 s2, 0x90
	v_lshl_add_u32 v4, v133, 6, v4
	v_lshlrev_b32_e32 v1, 4, v1
	v_lshlrev_b32_e32 v2, 4, v2
	v_and_or_b32 v1, v1, 48, v4
	v_mad_u64_u32 v[4:5], s[4:5], v133, s2, v[2:3]
	v_and_b32_e32 v8, 64, v0
	v_lshlrev_b32_e32 v116, 4, v3
	v_lshlrev_b32_e32 v118, 3, v3
	v_lshlrev_b32_e32 v5, 2, v3
	v_xor_b32_e32 v3, 32, v0
	v_add_u32_e32 v8, 64, v8
	v_cmp_lt_i32_e32 vcc, v3, v8
	v_mov_b32_e32 v80, 0
	v_readlane_b32 s4, v254, 47
	v_mad_u32_u24 v6, v132, s2, v116
	s_lshl_b32 s2, s95, 5
	v_cndmask_b32_e32 v0, v0, v3, vcc
	v_mov_b32_e32 v3, v80
	v_readlane_b32 s5, v254, 48
	s_and_b32 s16, s2, 32
	v_lshlrev_b32_e32 v136, 2, v0
	v_lshl_add_u64 v[120:121], s[4:5], 0, v[2:3]
	v_sub_u32_e32 v0, v5, v132
	v_mov_b64_e32 v[122:123], s[4:5]
	s_mov_b32 s4, 0x3f803f80
	s_lshr_b32 s17, s94, 7
	v_ashrrev_i32_e32 v119, 31, v118
	v_add_u32_e32 v134, 0x8000, v133
	v_add_u32_e32 v135, 0x8040, v133
	v_ashrrev_i32_e32 v117, 31, v116
	v_subrev_u32_e32 v137, s16, v0
	s_movk_i32 s18, 0xc00
	v_add_u32_e32 v138, 0, v4
	v_add_u32_e32 v139, 0, v1
	s_movk_i32 s19, 0xfefe
	s_mov_b32 s5, s4
	s_mov_b32 s6, s4
	s_mov_b32 s7, s4
	v_mov_b32_e32 v125, 0xbe38aa3b
	s_mov_b32 s20, 0xc3e00000
	v_add_u32_e32 v140, 0, v6
	v_mov_b32_e32 v141, 0xf149f2ca
	v_add_u32_e32 v142, 0, v7
	v_mov_b32_e32 v143, 0x43e00000
	s_mov_b32 s12, s96
	s_mov_b32 s21, 0
	s_branch .LBB0_257

.LBB0_284:
	s_setprio 0
	v_readlane_b32 s2, v254, 0
	v_readlane_b32 s3, v254, 1
	s_load_dwordx2 s[2:3], s[2:3], 0xd8
	s_waitcnt lgkmcnt(0)
	s_cmp_gt_i32 s3, 4
	s_cselect_b64 s[2:3], -1, 0
	s_and_b64 s[0:1], s[0:1], s[2:3]
	s_andn2_b64 vcc, exec, s[0:1]
	s_cbranch_vccnz .LBB0_340
	s_waitcnt vmcnt(0)
	s_cmp_gt_u32 s94, 63
	s_barrier
	s_cbranch_scc1 .LBB0_339
	v_mbcnt_lo_u32_b32 v0, -1, 0
	v_mbcnt_hi_u32_b32 v0, -1, v0
	v_cmp_eq_u32_e32 vcc, 0, v0
	s_and_saveexec_b64 s[0:1], vcc
	s_cbranch_execz .LBB0_338
	s_add_i32 s4, 0, 0x20020
	v_mov_b32_e32 v0, s4
	s_waitcnt vmcnt(0) expcnt(0) lgkmcnt(0)
	ds_read_b32 v2, v0
	s_add_i32 s4, 0, 0x20024
	v_mov_b32_e32 v0, s4
	ds_read_b32 v0, v0
	s_waitcnt lgkmcnt(1)
	v_cmp_ne_u32_e32 vcc, 0, v2
	s_cbranch_vccnz .LBB0_302
	v_readlane_b32 s4, v254, 2
	v_readlane_b32 s10, v254, 0
	v_readlane_b32 s5, v254, 3
	v_readlane_b32 s11, v254, 1
	s_load_dwordx2 s[8:9], s[4:5], 0x4
	s_mov_b32 s46, 1
	s_load_dword s10, s[10:11], 0xe8
	s_add_u32 s4, s88, 0x4200
	s_addc_u32 s5, s89, 0
	s_add_u32 s6, s88, 0x4400
	s_addc_u32 s7, s89, 0
	s_waitcnt lgkmcnt(0)
	s_mul_i32 s33, s8, s10
	s_add_u32 s8, s88, 0x4500
	s_mul_i32 s33, s33, s9
	s_addc_u32 s9, s89, 0
	s_add_u32 s10, s88, 0x4600
	s_addc_u32 s11, s89, 0
	s_add_u32 s12, s88, 0x4700
	s_addc_u32 s13, s89, 0
	s_add_u32 s14, s88, 0x4800
	s_addc_u32 s15, s89, 0
	s_add_u32 s16, s88, 0x4900
	s_addc_u32 s17, s89, 0
	s_add_u32 s18, s88, 0x4a00
	s_addc_u32 s19, s89, 0
	s_add_u32 s20, s88, 0x4b00
	s_addc_u32 s21, s89, 0
	s_add_u32 s22, s88, 0x4c00
	s_addc_u32 s23, s89, 0
	s_add_u32 s24, s88, 0x4d00
	s_addc_u32 s25, s89, 0
	s_add_u32 s26, s88, 0x4e00
	s_addc_u32 s27, s89, 0
	s_add_u32 s28, s88, 0x4f00
	s_addc_u32 s29, s89, 0
	s_add_u32 s30, s88, 0x5000
	s_addc_u32 s31, s89, 0
	s_add_u32 s34, s88, 0x5100
	s_addc_u32 s35, s89, 0
	s_add_u32 s36, s88, 0x5200
	s_addc_u32 s37, s89, 0
	s_add_u32 s38, s88, 0x5300
	s_addc_u32 s39, s89, 0
	v_mov_b32_e32 v16, 0
	s_branch .LBB0_290

.LBB0_1551:
	v_readlane_b32 s0, v254, 0
	v_readlane_b32 s1, v254, 1
	s_load_dwordx2 s[0:1], s[0:1], 0xd8
	s_waitcnt lgkmcnt(0)
	s_cmp_lt_i32 s0, 19
	s_cselect_b64 s[0:1], -1, 0
	s_and_b64 s[0:1], s[0:1], s[2:3]
	v_writelane_b32 v255, s0, 11
	s_andn2_b64 vcc, exec, s[0:1]
	s_nop 0
	v_writelane_b32 v255, s1, 12
	s_cbranch_vccnz .LBB0_1636
	s_cmp_gt_u32 s95, 3
	s_cbranch_scc0 .Lattp_18
	s_setprio 1
.Lattp_18:
	v_mbcnt_lo_u32_b32 v0, -1, 0
	v_mbcnt_hi_u32_b32 v2, -1, v0
	s_mov_b32 s83, 0
	v_mov_b32_e32 v0, v2
	s_cmpk_gt_i32 s96, 0x83f
	s_cbranch_scc1 .LBB0_1636
	v_lshrrev_b32_e32 v1, 3, v0
	v_bfe_u32 v4, v0, 2, 2
	s_mov_b32 s1, 0x3fffffc
	v_and_or_b32 v1, v1, s1, v4
	v_lshlrev_b32_e32 v4, 2, v0
	v_and_b32_e32 v5, 16, v0
	v_and_or_b32 v4, v4, 12, v5
	s_and_b32 s0, s94, 0xffffffc0
	v_lshlrev_b32_e32 v4, 1, v4
	v_add_u32_e32 v162, s0, v0
	v_lshl_or_b32 v166, v1, 6, v4
	v_bfe_u32 v4, v0, 2, 1
	v_ashrrev_i32_e32 v164, 3, v162
	v_mul_u32_u24_e32 v4, 0x1040, v4
	v_and_b32_e32 v163, 31, v0
	v_ashrrev_i32_e32 v3, 5, v0
	v_and_b32_e32 v1, 7, v0
	v_lshl_add_u32 v4, v164, 6, v4
	v_lshlrev_b32_e32 v0, 4, v0
	v_writelane_b32 v255, s92, 13
	v_lshlrev_b32_e32 v154, 4, v3
	s_movk_i32 s0, 0x90
	v_and_or_b32 v6, v0, 48, v4
	v_lshlrev_b32_e32 v4, 4, v1
	v_writelane_b32 v255, s93, 14
	v_mad_u32_u24 v165, v163, s0, v154
	v_mad_u64_u32 v[0:1], s[0:1], v164, s0, v[4:5]
	v_writelane_b32 v255, s95, 15
	s_lshr_b32 s1, s94, 7
	s_lshl_b32 s0, s95, 5
	v_writelane_b32 v255, s1, 16
	v_writelane_b32 v255, s0, 17
	s_add_i32 s0, s0, 0x8000
	v_writelane_b32 v255, s0, 18
	s_bfe_u32 s0, s94, 0x10006
	s_lshl_b32 s1, s0, 5
	v_or_b32_e32 v1, s1, v163
	v_lshlrev_b32_e32 v156, 3, v3
	v_med3_u32 v1, v1, 8, 56
	v_lshlrev_b32_e32 v3, 2, v3
	v_sub_u32_e32 v1, v3, v1
	v_add_u32_e32 v7, 40, v1
	v_cmp_gt_u32_e64 s[12:13], 16, v7
	v_add_u32_e32 v7, 41, v1
	v_cmp_gt_u32_e64 s[14:15], 16, v7
	v_add_u32_e32 v7, 42, v1
	v_cmp_gt_u32_e64 s[16:17], 16, v7
	v_add_u32_e32 v7, 43, v1
	v_cmp_gt_u32_e64 s[18:19], 16, v7
	v_add_u32_e32 v7, 49, v1
	v_and_b32_e32 v9, 64, v2
	v_cmp_gt_u32_e64 s[40:41], 16, v7
	v_add_u32_e32 v7, 50, v1
	s_movk_i32 s3, 0x1d1
	v_xor_b32_e32 v8, 32, v2
	v_add_u32_e32 v9, 64, v9
	v_cmp_gt_u32_e64 s[42:43], 16, v7
	v_add_u32_e32 v7, 51, v1
	v_cmp_gt_i32_e64 s[36:37], s3, v162
	s_and_b32 s3, 64, s94
	v_cmp_lt_i32_e32 vcc, v8, v9
	v_cmp_gt_u32_e64 s[44:45], 16, v7
	v_add_u32_e32 v7, 56, v1
	s_cmp_eq_u32 s0, 0
	v_cndmask_b32_e32 v2, v2, v8, vcc
	v_cmp_gt_u32_e64 s[46:47], 16, v7
	v_add_u32_e32 v7, 57, v1
	s_movk_i32 s2, 0xffc0
	s_cselect_b64 s[92:93], -1, 0
	s_cmp_lg_u32 s3, 0
	v_lshlrev_b32_e32 v170, 2, v2
	v_and_b32_e32 v2, -16, v1
	s_movk_i32 s0, 0xffe0
	s_movk_i32 s3, 0xffd0
	v_cmp_gt_u32_e64 s[48:49], 16, v7
	v_add_u32_e32 v7, 58, v1
	v_writelane_b32 v255, s94, 19
	v_cmp_eq_u32_e64 s[4:5], s0, v2
	v_cmp_eq_u32_e64 s[38:39], s3, v2
	v_cmp_gt_u32_e64 s[20:21], 16, v7
	v_cmp_eq_u32_e64 s[30:31], s2, v2
	v_add_u32_e32 v2, 0x41, v1
	v_writelane_b32 v255, s20, 20
	v_cmp_gt_u32_e64 s[34:35], 16, v2
	v_add_u32_e32 v2, 0x42, v1
	v_writelane_b32 v255, s21, 21
	v_cmp_gt_u32_e64 s[20:21], 16, v2
	v_add_u32_e32 v2, 0x43, v1
	v_add_u32_e32 v5, 8, v1
	v_writelane_b32 v255, s20, 22
	v_add_u32_e32 v8, 33, v1
	v_cmp_gt_u32_e64 s[6:7], 16, v8
	v_writelane_b32 v255, s21, 23
	v_cmp_gt_u32_e64 s[20:21], 16, v2
	v_add_u32_e32 v2, 9, v1
	v_add_u32_e32 v8, 34, v1
	v_writelane_b32 v255, s20, 24
	v_cmp_gt_u32_e64 s[8:9], 16, v8
	v_add_u32_e32 v8, 35, v1
	v_writelane_b32 v255, s21, 25
	v_cmp_gt_u32_e64 s[20:21], 16, v5
	v_add_u32_e32 v7, 59, v1
	s_waitcnt vmcnt(2)
	v_mov_b32_e32 v114, 0
	v_writelane_b32 v255, s20, 26
	v_readlane_b32 s22, v254, 47
	v_mov_b32_e32 v5, v114
	v_writelane_b32 v255, s21, 27
	v_cmp_gt_u32_e64 s[20:21], 16, v2
	v_add_u32_e32 v2, 10, v1
	v_readlane_b32 s23, v254, 48
	v_writelane_b32 v255, s20, 28
	s_mov_b32 s24, s96
	v_lshl_add_u64 v[158:159], s[22:23], 0, v[4:5]
	v_writelane_b32 v255, s21, 29
	v_cmp_gt_u32_e64 s[20:21], 16, v2
	v_add_u32_e32 v2, 11, v1
	v_cmp_gt_u32_e64 s[52:53], 16, v2
	v_add_u32_e32 v2, 17, v1
	v_cmp_gt_u32_e64 s[56:57], 16, v2
	v_add_u32_e32 v2, 18, v1
	v_cmp_gt_u32_e64 s[58:59], 16, v2
	v_add_u32_e32 v2, 19, v1
	v_writelane_b32 v255, s20, 30
	v_cmp_gt_u32_e64 s[60:61], 16, v2
	v_add_u32_e32 v2, 24, v1
	v_writelane_b32 v255, s21, 31
	s_movk_i32 s20, 0xffef
	v_cmp_gt_u32_e64 s[62:63], 16, v2
	v_add_u32_e32 v2, 25, v1
	v_cmp_lt_u32_e64 s[54:55], s20, v1
	v_cmp_gt_u32_e64 s[64:65], 16, v2
	v_add_u32_e32 v2, 26, v1
	v_add_u32_e32 v1, 27, v1
	v_cmp_gt_u32_e64 s[68:69], 16, v1
	v_sub_u32_e32 v1, v3, v163
	v_subrev_u32_e32 v1, s1, v1
	s_movk_i32 s1, 0xffd9
	v_cmp_gt_u32_e64 s[66:67], 16, v2
	v_med3_i32 v2, v1, s1, -9
	v_lshl_add_u32 v2, v2, 2, 0
	s_movk_i32 s1, 0xffd8
	v_add_u32_e32 v171, 0x8b10, v2
	v_med3_i32 v2, v1, s1, -10
	v_lshl_add_u32 v2, v2, 2, 0
	s_movk_i32 s1, 0xffd7
	v_add_u32_e32 v172, 0x8b14, v2
	v_med3_i32 v2, v1, s1, -11
	v_lshl_add_u32 v2, v2, 2, 0
	s_movk_i32 s1, 0xffd6
	v_add_u32_e32 v173, 0x8b18, v2
	v_med3_i32 v2, v1, s1, -12
	v_lshl_add_u32 v2, v2, 2, 0
	v_add_u32_e32 v174, 0x8b1c, v2
	s_movk_i32 s1, 0xffd1
	v_not_b32_e32 v2, 16
	v_med3_i32 v2, v1, s1, v2
	v_lshl_add_u32 v2, v2, 2, 0
	v_add_u32_e32 v175, 0x8b30, v2
	v_not_b32_e32 v2, 17
	v_med3_i32 v2, v1, s3, v2
	v_lshl_add_u32 v2, v2, 2, 0
	v_add_u32_e32 v176, 0x8b34, v2
	s_movk_i32 s3, 0xffcf
	v_not_b32_e32 v2, 18
	v_med3_i32 v2, v1, s3, v2
	v_lshl_add_u32 v2, v2, 2, 0
	v_add_u32_e32 v177, 0x8b38, v2
	s_movk_i32 s3, 0xffce
	v_not_b32_e32 v2, 19
	v_med3_i32 v2, v1, s3, v2
	v_lshl_add_u32 v2, v2, 2, 0
	v_add_u32_e32 v178, 0x8b3c, v2
	s_movk_i32 s21, 0xffc9
	v_not_b32_e32 v2, 24
	v_med3_i32 v2, v1, s21, v2
	v_lshl_add_u32 v2, v2, 2, 0
	v_add_u32_e32 v179, 0x8b50, v2
	s_movk_i32 s22, 0xffc8
	v_not_b32_e32 v2, 25
	v_med3_i32 v2, v1, s22, v2
	v_lshl_add_u32 v2, v2, 2, 0
	v_add_u32_e32 v180, 0x8b54, v2
	s_movk_i32 s22, 0xffc7
	v_not_b32_e32 v2, 26
	v_med3_i32 v2, v1, s22, v2
	v_lshl_add_u32 v2, v2, 2, 0
	v_add_u32_e32 v181, 0x8b58, v2
	s_movk_i32 s22, 0xffc6
	v_not_b32_e32 v2, 27
	v_med3_i32 v2, v1, s22, v2
	v_lshl_add_u32 v2, v2, 2, 0
	v_add_u32_e32 v182, 0x8b5c, v2
	s_movk_i32 s23, 0xffc1
	v_not_b32_e32 v2, 32
	v_med3_i32 v2, v1, s23, v2
	v_lshl_add_u32 v2, v2, 2, 0
	s_waitcnt vmcnt(0)
	v_add_u32_e32 v183, 0x8b70, v2
	v_not_b32_e32 v2, 33
	v_med3_i32 v2, v1, s2, v2
	v_lshl_add_u32 v2, v2, 2, 0
	v_add_u32_e32 v184, 0x8b74, v2
	s_movk_i32 s2, 0xffbf
	v_not_b32_e32 v2, 34
	v_med3_i32 v2, v1, s2, v2
	v_lshl_add_u32 v2, v2, 2, 0
	v_add_u32_e32 v185, 0x8b78, v2
	s_movk_i32 s2, 0xffbe
	v_not_b32_e32 v2, 35
	v_med3_i32 v2, v1, s2, v2
	v_lshl_add_u32 v2, v2, 2, 0
	v_add_u32_e32 v186, 0x8b7c, v2
	s_movk_i32 s2, 0xffb9
	v_not_b32_e32 v2, 40
	v_med3_i32 v2, v1, s2, v2
	v_lshl_add_u32 v2, v2, 2, 0
	v_add_u32_e32 v187, 0x8b90, v2
	s_movk_i32 s2, 0xffb8
	v_not_b32_e32 v2, 41
	v_med3_i32 v2, v1, s2, v2
	v_lshl_add_u32 v2, v2, 2, 0
	v_add_u32_e32 v188, 0x8b94, v2
	s_movk_i32 s2, 0xffb7
	v_not_b32_e32 v2, 42
	v_med3_i32 v2, v1, s2, v2
	v_lshl_add_u32 v2, v2, 2, 0
	v_add_u32_e32 v189, 0x8b98, v2
	s_movk_i32 s2, 0xffb6
	v_not_b32_e32 v2, 43
	v_med3_i32 v2, v1, s2, v2
	v_lshl_add_u32 v2, v2, 2, 0
	v_add_u32_e32 v190, 0x8b9c, v2
	v_med3_i32 v2, v1, -15, 15
	v_lshl_add_u32 v2, v2, 2, 0
	v_add_u32_e32 v191, 0x8ab0, v2
	v_med3_i32 v2, v1, -16, 14
	v_lshl_add_u32 v2, v2, 2, 0
	v_add_u32_e32 v192, 0x8ab4, v2
	v_med3_i32 v2, v1, s20, 13
	s_movk_i32 s1, 0xffee
	v_lshl_add_u32 v2, v2, 2, 0
	v_add_u32_e32 v193, 0x8ab8, v2
	v_med3_i32 v2, v1, s1, 12
	v_lshl_add_u32 v2, v2, 2, 0
	s_movk_i32 s1, 0xffe9
	v_add_u32_e32 v194, 0x8abc, v2
	v_med3_i32 v2, v1, s1, 7
	v_lshl_add_u32 v2, v2, 2, 0
	s_movk_i32 s1, 0xffe8
	v_add_u32_e32 v195, 0x8ad0, v2
	v_med3_i32 v2, v1, s1, 6
	s_movk_i32 s3, 0xffe7
	v_lshl_add_u32 v2, v2, 2, 0
	v_add_u32_e32 v196, 0x8ad4, v2
	v_med3_i32 v2, v1, s3, 5
	s_movk_i32 s21, 0xffe6
	v_lshl_add_u32 v2, v2, 2, 0
	v_add_u32_e32 v197, 0x8ad8, v2
	v_med3_i32 v2, v1, s21, 4
	v_lshl_add_u32 v2, v2, 2, 0
	s_movk_i32 s1, 0xffe1
	v_add_u32_e32 v198, 0x8adc, v2
	v_med3_i32 v2, v1, s1, -1
	v_lshl_add_u32 v2, v2, 2, 0
	v_add_u32_e32 v199, 0x8af0, v2
	v_med3_i32 v2, v1, s0, -2
	s_movk_i32 s22, 0xffdf
	s_movk_i32 s23, 0xffde
	v_lshl_add_u32 v2, v2, 2, 0
	v_add_u32_e32 v200, 0x8af4, v2
	v_med3_i32 v2, v1, s22, -3
	v_med3_i32 v1, v1, s23, -4
	v_lshl_add_u32 v2, v2, 2, 0
	v_lshl_add_u32 v1, v1, 2, 0
	v_ashrrev_i32_e32 v157, 31, v156
	v_add_u32_e32 v167, 0x8000, v164
	v_lshl_add_u32 v168, v162, 2, 0
	v_add_u32_e32 v169, 0x8040, v164
	s_cselect_b64 s[96:97], -1, 0
	v_ashrrev_i32_e32 v155, 31, v154
	v_cmp_gt_u32_e64 s[10:11], 16, v8
	v_cmp_gt_u32_e64 s[28:29], 16, v7
	v_add_u32_e32 v201, 0x8af8, v2
	v_add_u32_e32 v202, 0x8afc, v1
	s_movk_i32 s33, 0x1800
	s_mov_b32 s72, 0x3f803f80
	s_mov_b32 s2, 0xc3e00000
	v_mov_b32_e32 v203, 0x79
	v_mov_b32_e32 v204, 0x7c
	v_add_u32_e32 v205, 0, v0
	v_add_u32_e32 v206, 0, v6
	v_mov_b32_e32 v207, 0xf149f2ca
	v_mov_b32_e32 v118, 0x3f803f80
	v_mov_b32_e32 v208, 0x43e00000
	v_writelane_b32 v255, s24, 32
	s_mov_b32 s21, s24
	s_mov_b32 s3, 0
	s_branch .LBB0_1556

.LBB0_1636:
	s_setprio 0
	v_readlane_b32 s0, v254, 0
	v_readlane_b32 s1, v254, 1
	s_load_dwordx2 s[0:1], s[0:1], 0xd8
	v_readlane_b32 s2, v255, 11
	v_readlane_b32 s3, v255, 12
	s_waitcnt lgkmcnt(0)
	s_cmp_gt_i32 s1, 19
	s_cselect_b64 s[0:1], -1, 0
	s_and_b64 s[2:3], s[2:3], s[0:1]
	s_andn2_b64 vcc, exec, s[2:3]
	s_cbranch_vccnz .LBB0_1692
	s_waitcnt vmcnt(0)
	s_cmp_gt_u32 s94, 63
	s_barrier
	s_cbranch_scc1 .LBB0_1691
	v_mbcnt_lo_u32_b32 v0, -1, 0
	v_mbcnt_hi_u32_b32 v0, -1, v0
	v_cmp_eq_u32_e32 vcc, 0, v0
	s_and_saveexec_b64 s[2:3], vcc
	s_cbranch_execz .LBB0_1690
	s_add_i32 s4, 0, 0x20020
	v_mov_b32_e32 v0, s4
	s_waitcnt vmcnt(0) expcnt(0) lgkmcnt(0)
	ds_read_b32 v2, v0
	s_add_i32 s4, 0, 0x20024
	v_mov_b32_e32 v0, s4
	ds_read_b32 v0, v0
	s_waitcnt lgkmcnt(1)
	v_cmp_ne_u32_e32 vcc, 0, v2
	s_cbranch_vccnz .LBB0_1654
	v_readlane_b32 s4, v254, 2
	v_readlane_b32 s10, v254, 0
	v_readlane_b32 s5, v254, 3
	v_readlane_b32 s11, v254, 1
	s_load_dwordx2 s[8:9], s[4:5], 0x4
	s_mov_b32 s46, 1
	s_load_dword s10, s[10:11], 0xe8
	s_add_u32 s4, s88, 0x4200
	s_addc_u32 s5, s89, 0
	s_add_u32 s6, s88, 0x4400
	s_addc_u32 s7, s89, 0
	s_waitcnt lgkmcnt(0)
	s_mul_i32 s33, s8, s10
	s_add_u32 s8, s88, 0x4500
	s_mul_i32 s33, s33, s9
	s_addc_u32 s9, s89, 0
	s_add_u32 s10, s88, 0x4600
	s_addc_u32 s11, s89, 0
	s_add_u32 s12, s88, 0x4700
	s_addc_u32 s13, s89, 0
	s_add_u32 s14, s88, 0x4800
	s_addc_u32 s15, s89, 0
	s_add_u32 s16, s88, 0x4900
	s_addc_u32 s17, s89, 0
	s_add_u32 s18, s88, 0x4a00
	s_addc_u32 s19, s89, 0
	s_add_u32 s20, s88, 0x4b00
	s_addc_u32 s21, s89, 0
	s_add_u32 s22, s88, 0x4c00
	s_addc_u32 s23, s89, 0
	s_add_u32 s24, s88, 0x4d00
	s_addc_u32 s25, s89, 0
	s_add_u32 s26, s88, 0x4e00
	s_addc_u32 s27, s89, 0
	s_add_u32 s28, s88, 0x4f00
	s_addc_u32 s29, s89, 0
	s_add_u32 s30, s88, 0x5000
	s_addc_u32 s31, s89, 0
	s_add_u32 s34, s88, 0x5100
	s_addc_u32 s35, s89, 0
	s_add_u32 s36, s88, 0x5200
	s_addc_u32 s37, s89, 0
	s_add_u32 s38, s88, 0x5300
	s_addc_u32 s39, s89, 0
	v_mov_b32_e32 v16, 0
	s_branch .LBB0_1642

.LBB0_2210:
	v_readlane_b32 s0, v254, 0
	v_readlane_b32 s1, v254, 1
	s_load_dwordx2 s[0:1], s[0:1], 0xd8
	s_waitcnt lgkmcnt(0)
	s_cmp_lt_i32 s0, 26
	s_cselect_b64 s[0:1], -1, 0
	s_and_b64 s[0:1], s[0:1], s[2:3]
	s_andn2_b64 vcc, exec, s[0:1]
	s_cbranch_vccnz .LBB0_2237
	s_cmp_gt_u32 s95, 3
	s_cbranch_scc0 .Lattp_25
	s_setprio 1
.Lattp_25:
	v_mbcnt_lo_u32_b32 v0, -1, 0
	v_mbcnt_hi_u32_b32 v0, -1, v0
	s_mov_b32 s3, 0
	v_mov_b32_e32 v1, v0
	s_cmpk_gt_i32 s96, 0x7ff
	s_cbranch_scc1 .LBB0_2237
	s_and_b32 s2, s94, 0xffffffc0
	v_add_u32_e32 v2, s2, v1
	v_ashrrev_i32_e32 v133, 3, v2
	v_lshrrev_b32_e32 v2, 3, v1
	v_bfe_u32 v4, v1, 2, 2
	s_mov_b32 s4, 0x3fffffc
	v_and_or_b32 v2, v2, s4, v4
	v_lshlrev_b32_e32 v4, 2, v1
	v_and_b32_e32 v5, 16, v1
	v_and_or_b32 v4, v4, 12, v5
	v_lshlrev_b32_e32 v4, 1, v4
	v_lshl_or_b32 v7, v2, 6, v4
	v_bfe_u32 v4, v1, 2, 1
	v_and_b32_e32 v2, 7, v1
	v_mul_u32_u24_e32 v4, 0x1040, v4
	v_and_b32_e32 v132, 31, v1
	v_ashrrev_i32_e32 v3, 5, v1
	s_movk_i32 s2, 0x90
	v_lshl_add_u32 v4, v133, 6, v4
	v_lshlrev_b32_e32 v1, 4, v1
	v_lshlrev_b32_e32 v2, 4, v2
	v_and_or_b32 v1, v1, 48, v4
	v_mad_u64_u32 v[4:5], s[4:5], v133, s2, v[2:3]
	v_and_b32_e32 v8, 64, v0
	s_waitcnt vmcnt(6)
	v_lshlrev_b32_e32 v116, 4, v3
	v_lshlrev_b32_e32 v118, 3, v3
	v_lshlrev_b32_e32 v5, 2, v3
	v_xor_b32_e32 v3, 32, v0
	v_add_u32_e32 v8, 64, v8
	v_cmp_lt_i32_e32 vcc, v3, v8
	v_mov_b32_e32 v80, 0
	v_readlane_b32 s4, v254, 47
	v_mad_u32_u24 v6, v132, s2, v116
	s_lshl_b32 s2, s95, 5
	v_cndmask_b32_e32 v0, v0, v3, vcc
	v_mov_b32_e32 v3, v80
	v_readlane_b32 s5, v254, 48
	s_and_b32 s16, s2, 32
	v_lshlrev_b32_e32 v136, 2, v0
	s_waitcnt vmcnt(5)
	v_lshl_add_u64 v[120:121], s[4:5], 0, v[2:3]
	v_sub_u32_e32 v0, v5, v132
	v_mov_b64_e32 v[122:123], s[4:5]
	s_mov_b32 s4, 0x3f803f80
	s_lshr_b32 s17, s94, 7
	v_ashrrev_i32_e32 v119, 31, v118
	v_add_u32_e32 v134, 0x8000, v133
	v_add_u32_e32 v135, 0x8040, v133
	v_ashrrev_i32_e32 v117, 31, v116
	v_subrev_u32_e32 v137, s16, v0
	s_movk_i32 s18, 0xc00
	s_waitcnt vmcnt(3)
	v_add_u32_e32 v138, 0, v4
	v_add_u32_e32 v139, 0, v1
	s_movk_i32 s19, 0xfefe
	s_mov_b32 s5, s4
	s_mov_b32 s6, s4
	s_mov_b32 s7, s4
	v_mov_b32_e32 v125, 0xbe38aa3b
	s_mov_b32 s20, 0xc3e00000
	v_add_u32_e32 v140, 0, v6
	v_mov_b32_e32 v141, 0xf149f2ca
	s_waitcnt vmcnt(2)
	v_add_u32_e32 v142, 0, v7
	v_mov_b32_e32 v143, 0x43e00000
	s_mov_b32 s21, s96
	s_mov_b32 s2, s96
	s_mov_b32 s22, 0
	s_branch .LBB0_2214

.LBB0_2237:
	s_setprio 0
	v_readlane_b32 s2, v254, 0
	v_readlane_b32 s3, v254, 1
	s_load_dwordx2 s[2:3], s[2:3], 0xd8
	s_waitcnt lgkmcnt(0)
	s_cmp_gt_i32 s3, 26
	s_cselect_b64 s[2:3], -1, 0
	s_and_b64 s[0:1], s[0:1], s[2:3]
	s_andn2_b64 vcc, exec, s[0:1]
	s_cbranch_vccnz .LBB0_2293
	s_waitcnt vmcnt(0)
	s_cmp_gt_u32 s94, 63
	s_barrier
	s_cbranch_scc1 .LBB0_2292
	v_mbcnt_lo_u32_b32 v0, -1, 0
	v_mbcnt_hi_u32_b32 v0, -1, v0
	v_cmp_eq_u32_e32 vcc, 0, v0
	s_and_saveexec_b64 s[0:1], vcc
	s_cbranch_execz .LBB0_2291
	s_add_i32 s4, 0, 0x20020
	v_mov_b32_e32 v0, s4
	s_waitcnt vmcnt(0) expcnt(0) lgkmcnt(0)
	ds_read_b32 v2, v0
	s_add_i32 s4, 0, 0x20024
	v_mov_b32_e32 v0, s4
	ds_read_b32 v0, v0
	s_waitcnt lgkmcnt(1)
	v_cmp_ne_u32_e32 vcc, 0, v2
	s_cbranch_vccnz .LBB0_2255
	v_readlane_b32 s4, v254, 2
	v_readlane_b32 s10, v254, 0
	v_readlane_b32 s5, v254, 3
	v_readlane_b32 s11, v254, 1
	s_load_dwordx2 s[8:9], s[4:5], 0x4
	s_mov_b32 s46, 1
	s_load_dword s10, s[10:11], 0xe8
	s_add_u32 s4, s88, 0x4200
	s_addc_u32 s5, s89, 0
	s_add_u32 s6, s88, 0x4400
	s_addc_u32 s7, s89, 0
	s_waitcnt lgkmcnt(0)
	s_mul_i32 s33, s8, s10
	s_add_u32 s8, s88, 0x4500
	s_mul_i32 s33, s33, s9
	s_addc_u32 s9, s89, 0
	s_add_u32 s10, s88, 0x4600
	s_addc_u32 s11, s89, 0
	s_add_u32 s12, s88, 0x4700
	s_addc_u32 s13, s89, 0
	s_add_u32 s14, s88, 0x4800
	s_addc_u32 s15, s89, 0
	s_add_u32 s16, s88, 0x4900
	s_addc_u32 s17, s89, 0
	s_add_u32 s18, s88, 0x4a00
	s_addc_u32 s19, s89, 0
	s_add_u32 s20, s88, 0x4b00
	s_addc_u32 s21, s89, 0
	s_add_u32 s22, s88, 0x4c00
	s_addc_u32 s23, s89, 0
	s_add_u32 s24, s88, 0x4d00
	s_addc_u32 s25, s89, 0
	s_add_u32 s26, s88, 0x4e00
	s_addc_u32 s27, s89, 0
	s_add_u32 s28, s88, 0x4f00
	s_addc_u32 s29, s89, 0
	s_add_u32 s30, s88, 0x5000
	s_addc_u32 s31, s89, 0
	s_add_u32 s34, s88, 0x5100
	s_addc_u32 s35, s89, 0
	s_add_u32 s36, s88, 0x5200
	s_addc_u32 s37, s89, 0
	s_add_u32 s38, s88, 0x5300
	s_addc_u32 s39, s89, 0
	v_mov_b32_e32 v16, 0
	s_branch .LBB0_2243
